# tail-aware stagger: delay index wg>>5 (8 groups x 1.5us) so the most delayed groups have one unit fewer
# speedup vs baseline: 1.0210x; 1.0032x over previous
.LBB0_1847:
	s_or_b64 exec, exec, s[0:1]
	v_readlane_b32 s0, v254, 4
	s_mov_b32 s2, 0
	s_mov_b32 s4, s0
	v_readlane_b32 s54, v254, 2
	v_readlane_b32 s0, v254, 3
	s_waitcnt lgkmcnt(0)
	s_barrier
	s_lshr_b32 s98, s4, 5
	s_and_b32 s98, s98, 7
	s_cmp_eq_u32 s98, 0
	s_cbranch_scc1 .Lstg_done
